# fused conversion in GEMM1 epilogues + workgroups start GEMM1 staggered in 4 groups (s_sleep) so the conversion bursts of different workgroups do not coincide
# speedup vs baseline: 1.0105x; 1.0040x over previous
.LBB0_1235:
	s_andn2_b64 vcc, exec, s[0:1]
	s_cbranch_vccnz .LBB0_1338
	s_cmp_lg_u32 s52, 3
	v_readlane_b32 s4, v253, 4
	s_cselect_b64 s[0:1], -1, 0
	v_readlane_b32 s5, v253, 5
	s_and_b64 s[0:1], s[4:5], s[0:1]
	v_readlane_b32 s4, v254, 32
	v_readlane_b32 s5, v254, 33
	s_and_b64 s[4:5], s[4:5], s[0:1]
	v_readlane_b32 s44, v253, 0
	v_readlane_b32 s45, v253, 1
	s_andn2_b64 vcc, exec, s[4:5]
	s_mov_b64 s[4:5], -1
	s_cbranch_vccz .LBB0_1258
	v_mov_b32_e32 v4, v0
	s_movk_i32 s5, 0x3c0
	v_readfirstlane_b32 s23, v4
	v_and_b32_e32 v2, 48, v4
	v_lshlrev_b32_e32 v3, 6, v4
	s_ashr_i32 s25, s23, 8
	v_and_or_b32 v2, v3, s5, v2
	v_lshlrev_b32_e32 v3, 2, v4
	s_ashr_i32 s24, s23, 6
	s_lshl_b32 s4, s25, 13
	v_and_b32_e32 v5, 32, v3
	v_bitop3_b32 v3, v2, s4, v5 bitop3:0xde
	s_lshl_b32 s4, s24, 5
	s_and_b32 s6, s4, 0x60
	s_lshl_b32 s4, s6, 7
	v_bitop3_b32 v2, s4, v2, v5 bitop3:0xf6
	v_readlane_b32 s4, v254, 34
	v_readlane_b32 s5, v254, 35
	v_or_b32_e32 v2, 0x10000, v2
	s_andn2_b64 vcc, exec, s[4:5]
	s_cbranch_vccnz .LBB0_1257
	s_cmp_lt_u32 s52, 3
	s_cbranch_scc0 .Lfz_nostag
	s_bfe_u32 s4, s88, 0x20003
	s_cmp_eq_u32 s4, 0
	s_cbranch_scc1 .Lfz_nostag
.Lfz_stag:
	s_sleep 127
	s_add_i32 s4, s4, -1
	s_cmp_lg_u32 s4, 0
	s_cbranch_scc1 .Lfz_stag
.Lfz_nostag:
	s_load_dwordx2 s[40:41], s[44:45], 0xa0
	s_lshl_b32 s7, s25, 6
	v_lshlrev_b32_e32 v5, 4, v4
	v_and_b32_e32 v6, 32, v4
	v_bfe_u32 v8, v4, 2, 26
	s_waitcnt lgkmcnt(0)
	s_add_u32 s42, s40, 0x33900000
	s_addc_u32 s43, s41, 0
	s_lshl_b32 s4, s52, 27
	s_add_u32 s4, s40, s4
	s_addc_u32 s5, s41, 0
	v_lshrrev_b32_e32 v9, 1, v4
	v_lshrrev_b32_e32 v10, 5, v4
	v_bfe_u32 v11, v5, 6, 2
	s_add_u32 s8, s4, 0x3900000
	v_bitop3_b32 v6, v5, v6, 48 bitop3:0x6c
	v_and_b32_e32 v8, 0x3fffc0, v8
	v_and_b32_e32 v9, 24, v9
	v_and_or_b32 v10, v10, 4, v11
	s_addc_u32 s9, s5, 0
	v_lshrrev_b32_e32 v7, 3, v4
	v_or3_b32 v8, v10, v9, v8
	v_and_or_b32 v9, v4, 64, v6
	v_bfe_u32 v4, v5, 6, 4
	s_mov_b32 s5, 0x1fffff0
	v_and_or_b32 v4, v7, s5, v4
	v_readlane_b32 s5, v254, 37
	s_add_u32 s46, s40, 0x37d00000
	s_addc_u32 s47, s41, 0
	v_add_u32_e32 v4, s5, v4
	v_ashrrev_i32_e32 v5, 31, v4
	v_lshl_add_u64 v[6:7], v[4:5], 2, s[46:47]
	global_load_dword v5, v[6:7], off
	s_lshl_b32 s4, s24, 10
	v_readlane_b32 s12, v254, 40
	v_readlane_b32 s13, v254, 41
	s_add_u32 s74, s8, s12
	v_lshl_or_b32 v194, v8, 10, v9
	s_addc_u32 s75, s9, s13
	s_add_i32 s10, s4, 0
	s_add_i32 s12, s10, 0x10000
	s_mov_b64 s[4:5], s[74:75]
	s_mov_b32 m0, s12
	s_waitcnt vmcnt(0)
	v_lshl_or_b32 v195, v5, 10, v9
	global_load_dword v5, v[6:7], off offset:256
	v_add_u32_e32 v6, 0x80, v4
	v_ashrrev_i32_e32 v7, 31, v6
	v_lshl_add_u64 v[6:7], v[6:7], 2, s[46:47]
	v_add_u32_e32 v4, 0xc0, v4
	s_waitcnt vmcnt(0)
	v_lshl_or_b32 v196, v5, 10, v9
	global_load_dword v5, v[6:7], off
	s_waitcnt vmcnt(0)
	v_lshl_or_b32 v197, v5, 10, v9
	v_ashrrev_i32_e32 v5, 31, v4
	v_lshl_add_u64 v[4:5], v[4:5], 2, s[46:47]
	global_load_dword v4, v[4:5], off
	s_waitcnt vmcnt(0)
	v_lshl_or_b32 v198, v4, 10, v9
	v_mov_b32_e32 v4, v194
	s_nop 0
	global_load_lds_dwordx4 v4, s[4:5]
	s_add_u32 s4, s74, 0x20000
	s_addc_u32 s5, s75, 0
	v_mov_b32_e32 v4, v194
	s_add_i32 s13, s10, 0x12000
	s_mov_b32 m0, s13
	s_add_i32 s14, s10, 0x14000
	global_load_lds_dwordx4 v4, s[4:5]
	s_add_u32 s4, s74, 0x8000
	s_addc_u32 s5, s75, 0
	v_mov_b32_e32 v4, v194
	s_mov_b32 m0, s14
	s_nop 0
	global_load_lds_dwordx4 v4, s[4:5]
	s_add_u32 s4, s74, 0x28000
	s_addc_u32 s5, s75, 0
	v_mov_b32_e32 v4, v194
	s_add_i32 s15, s10, 0x16000
	s_mov_b32 m0, s15
	s_add_i32 s16, s10, 0x2000
	global_load_lds_dwordx4 v4, s[4:5]
	s_mov_b64 s[4:5], s[42:43]
	v_mov_b32_e32 v4, v195
	s_mov_b32 m0, s10
	s_add_i32 s17, s10, 0x4000
	global_load_lds_dwordx4 v4, s[4:5]
	v_mov_b32_e32 v4, v196
	s_mov_b32 m0, s16
	s_add_i32 s26, s10, 0x6000
	global_load_lds_dwordx4 v4, s[4:5]
	s_mov_b64 s[4:5], s[42:43]
	v_mov_b32_e32 v4, v197
	s_mov_b32 m0, s17
	s_cmp_eq_u32 s25, 1
	global_load_lds_dwordx4 v4, s[4:5]
	v_mov_b32_e32 v4, v198
	s_mov_b32 m0, s26
	s_cselect_b64 s[48:49], -1, 0
	global_load_lds_dwordx4 v4, s[4:5]
	s_cmp_lg_u32 s25, 1
	s_cbranch_scc1 .LBB0_1240
	s_barrier
